# final RMSNorm rewrite with sc1 (write-through) on the f32 output stores
# speedup vs baseline: 1.0006x; 1.0006x over previous
.LBB0_3638:
	s_or_b64 exec, exec, s[6:7]
	s_lshr_b32 s1, s97, 3
	s_mul_i32 s1, s1, s64
	v_readlane_b32 s3, v254, 12
	s_and_b32 s0, s97, 7
	s_add_i32 s1, s1, s3
	s_cmp_eq_u32 s0, 0
	s_cselect_b32 s0, s1, s2
	s_waitcnt lgkmcnt(0)
	s_barrier
	s_lshl_b32 s1, s0, 3
	s_nop 0
	v_readfirstlane_b32 s0, v0
	s_lshl_b32 s13, s97, 3
	s_ashr_i32 s2, s0, 6
	s_add_i32 s12, s2, s1
	s_cmp_lt_i32 s12, 0x10000
	s_cbranch_scc0 .LBB0_3641
	s_load_dwordx4 s[4:7], s[90:91], 0xc0
	s_load_dwordx2 s[8:9], s[90:91], 0x28
	v_and_b32_e32 v1, 63, v0
	v_lshlrev_b32_e32 v2, 4, v1
	v_lshlrev_b32_e32 v3, 3, v1
	v_and_b32_e32 v4, 15, v1
	v_lshlrev_b32_e32 v4, 18, v4
	v_mov_b32_e32 v5, 0x358637bd
	s_lshl_b32 s20, s13, 2
	s_lshl_b32 s21, s13, 11
	s_lshl_b32 s22, s13, 12
	s_mul_i32 s23, s13, 7
	s_waitcnt lgkmcnt(0)
	global_load_dwordx4 v[8:11], v2, s[8:9] offset:0
	global_load_dwordx4 v[12:15], v2, s[8:9] offset:1024
	global_load_dwordx4 v[16:19], v2, s[8:9] offset:2048
	global_load_dwordx4 v[20:23], v2, s[8:9] offset:3072
	s_ashr_i32 s15, s12, 31
	s_mov_b32 s14, s12
	s_lshl_b64 s[16:17], s[14:15], 2
	s_add_u32 s16, s16, 0x72000000
	s_addc_u32 s17, s17, 0
	s_add_u32 s16, s16, s6
	s_addc_u32 s17, s17, s7
	s_lshl_b64 s[18:19], s[14:15], 11
	s_add_u32 s18, s18, 0x26c00000
	s_addc_u32 s19, s19, 0
	s_add_u32 s18, s18, s6
	s_addc_u32 s19, s19, s7
	s_lshl_b64 s[24:25], s[14:15], 12
	s_add_u32 s24, s24, s4
	s_addc_u32 s25, s25, s5
	s_add_i32 s14, s12, s23
	s_cmp_lt_i32 s14, 0x10000
	s_cbranch_scc0 .Lfin_tail
	s_mov_b64 s[26:27], s[16:17]
	s_mov_b64 s[28:29], s[18:19]
	global_load_dword v40, v4, s[26:27]
	global_load_dwordx2 v[32:33], v3, s[28:29] offset:0
	global_load_dwordx2 v[34:35], v3, s[28:29] offset:512
	global_load_dwordx2 v[36:37], v3, s[28:29] offset:1024
	global_load_dwordx2 v[38:39], v3, s[28:29] offset:1536
	s_add_u32 s16, s16, s20
	s_addc_u32 s17, s17, 0
	s_add_u32 s18, s18, s21
	s_addc_u32 s19, s19, 0
	s_add_i32 s12, s12, s13
	s_mov_b64 s[30:31], s[16:17]
	s_mov_b64 s[32:33], s[18:19]
	global_load_dword v50, v4, s[30:31]
	global_load_dwordx2 v[42:43], v3, s[32:33] offset:0
	global_load_dwordx2 v[44:45], v3, s[32:33] offset:512
	global_load_dwordx2 v[46:47], v3, s[32:33] offset:1024
	global_load_dwordx2 v[48:49], v3, s[32:33] offset:1536
	s_add_u32 s16, s16, s20
	s_addc_u32 s17, s17, 0
	s_add_u32 s18, s18, s21
	s_addc_u32 s19, s19, 0
	s_add_i32 s12, s12, s13
	s_mov_b64 s[26:27], s[16:17]
	s_mov_b64 s[28:29], s[18:19]
	global_load_dword v60, v4, s[26:27]
	global_load_dwordx2 v[52:53], v3, s[28:29] offset:0
	global_load_dwordx2 v[54:55], v3, s[28:29] offset:512
	global_load_dwordx2 v[56:57], v3, s[28:29] offset:1024
	global_load_dwordx2 v[58:59], v3, s[28:29] offset:1536
	s_add_u32 s16, s16, s20
	s_addc_u32 s17, s17, 0
	s_add_u32 s18, s18, s21
	s_addc_u32 s19, s19, 0
	s_add_i32 s12, s12, s13
	s_mov_b64 s[30:31], s[16:17]
	s_mov_b64 s[32:33], s[18:19]
	global_load_dword v70, v4, s[30:31]
	global_load_dwordx2 v[62:63], v3, s[32:33] offset:0
	global_load_dwordx2 v[64:65], v3, s[32:33] offset:512
	global_load_dwordx2 v[66:67], v3, s[32:33] offset:1024
	global_load_dwordx2 v[68:69], v3, s[32:33] offset:1536
	s_add_u32 s16, s16, s20
	s_addc_u32 s17, s17, 0
	s_add_u32 s18, s18, s21
	s_addc_u32 s19, s19, 0
	s_add_i32 s12, s12, s13
	s_mov_b64 s[26:27], s[16:17]
	s_mov_b64 s[28:29], s[18:19]
	global_load_dword v80, v4, s[26:27]
	global_load_dwordx2 v[72:73], v3, s[28:29] offset:0
	global_load_dwordx2 v[74:75], v3, s[28:29] offset:512
	global_load_dwordx2 v[76:77], v3, s[28:29] offset:1024
	global_load_dwordx2 v[78:79], v3, s[28:29] offset:1536
	s_add_u32 s16, s16, s20
	s_addc_u32 s17, s17, 0
	s_add_u32 s18, s18, s21
	s_addc_u32 s19, s19, 0
	s_add_i32 s12, s12, s13
	s_mov_b64 s[30:31], s[16:17]
	s_mov_b64 s[32:33], s[18:19]
	global_load_dword v90, v4, s[30:31]
	global_load_dwordx2 v[82:83], v3, s[32:33] offset:0
	global_load_dwordx2 v[84:85], v3, s[32:33] offset:512
	global_load_dwordx2 v[86:87], v3, s[32:33] offset:1024
	global_load_dwordx2 v[88:89], v3, s[32:33] offset:1536
	s_add_u32 s16, s16, s20
	s_addc_u32 s17, s17, 0
	s_add_u32 s18, s18, s21
	s_addc_u32 s19, s19, 0
	s_add_i32 s12, s12, s13
	s_mov_b64 s[26:27], s[16:17]
	s_mov_b64 s[28:29], s[18:19]
	global_load_dword v100, v4, s[26:27]
	global_load_dwordx2 v[92:93], v3, s[28:29] offset:0
	global_load_dwordx2 v[94:95], v3, s[28:29] offset:512
	global_load_dwordx2 v[96:97], v3, s[28:29] offset:1024
	global_load_dwordx2 v[98:99], v3, s[28:29] offset:1536
	s_add_u32 s16, s16, s20
	s_addc_u32 s17, s17, 0
	s_add_u32 s18, s18, s21
	s_addc_u32 s19, s19, 0
	s_add_i32 s12, s12, s13
	s_mov_b64 s[30:31], s[16:17]
	s_mov_b64 s[32:33], s[18:19]
	global_load_dword v110, v4, s[30:31]
	global_load_dwordx2 v[102:103], v3, s[32:33] offset:0
	global_load_dwordx2 v[104:105], v3, s[32:33] offset:512
	global_load_dwordx2 v[106:107], v3, s[32:33] offset:1024
	global_load_dwordx2 v[108:109], v3, s[32:33] offset:1536
	s_add_u32 s16, s16, s20
	s_addc_u32 s17, s17, 0
	s_add_u32 s18, s18, s21
	s_addc_u32 s19, s19, 0
	s_add_i32 s12, s12, s13
	s_waitcnt vmcnt(35)
	v_add_f32_dpp v112, v40, v40 quad_perm:[1,0,3,2] row_mask:0xf bank_mask:0xf
	s_mov_b64 s[34:35], s[24:25]
	s_add_u32 s24, s24, s22
	v_add_f32_dpp v112, v112, v112 quad_perm:[2,3,0,1] row_mask:0xf bank_mask:0xf
	s_addc_u32 s25, s25, 0
	s_nop 0
	v_add_f32_dpp v112, v112, v112 row_half_mirror row_mask:0xf bank_mask:0xf
	s_nop 1
	v_add_f32_dpp v112, v112, v112 row_mirror row_mask:0xf bank_mask:0xf
	v_fmamk_f32 v112, v112, 0x3a800000, v5
	v_rsq_f32_e32 v114, v112
	v_lshlrev_b32_e32 v116, 16, v32
	v_and_b32_e32 v117, 0xffff0000, v32
	v_lshlrev_b32_e32 v118, 16, v33
	v_and_b32_e32 v119, 0xffff0000, v33
	v_lshlrev_b32_e32 v120, 16, v34
	v_and_b32_e32 v121, 0xffff0000, v34
	v_lshlrev_b32_e32 v122, 16, v35
	v_and_b32_e32 v123, 0xffff0000, v35
	v_lshlrev_b32_e32 v124, 16, v36
	v_and_b32_e32 v125, 0xffff0000, v36
	v_lshlrev_b32_e32 v126, 16, v37
	v_and_b32_e32 v127, 0xffff0000, v37
	v_lshlrev_b32_e32 v128, 16, v38
	v_and_b32_e32 v129, 0xffff0000, v38
	v_lshlrev_b32_e32 v130, 16, v39
	v_and_b32_e32 v131, 0xffff0000, v39
	v_pk_mul_f32 v[116:117], v[114:115], v[116:117] op_sel_hi:[0,1]
	v_pk_mul_f32 v[118:119], v[114:115], v[118:119] op_sel_hi:[0,1]
	v_pk_mul_f32 v[120:121], v[114:115], v[120:121] op_sel_hi:[0,1]
	v_pk_mul_f32 v[122:123], v[114:115], v[122:123] op_sel_hi:[0,1]
	v_pk_mul_f32 v[124:125], v[114:115], v[124:125] op_sel_hi:[0,1]
	v_pk_mul_f32 v[126:127], v[114:115], v[126:127] op_sel_hi:[0,1]
	v_pk_mul_f32 v[128:129], v[114:115], v[128:129] op_sel_hi:[0,1]
	v_pk_mul_f32 v[130:131], v[114:115], v[130:131] op_sel_hi:[0,1]
	v_pk_mul_f32 v[132:133], v[8:9], v[116:117]
	v_pk_mul_f32 v[134:135], v[10:11], v[118:119]
	v_pk_mul_f32 v[136:137], v[12:13], v[120:121]
	v_pk_mul_f32 v[138:139], v[14:15], v[122:123]
	v_pk_mul_f32 v[140:141], v[16:17], v[124:125]
	v_pk_mul_f32 v[142:143], v[18:19], v[126:127]
	v_pk_mul_f32 v[144:145], v[20:21], v[128:129]
	v_pk_mul_f32 v[146:147], v[22:23], v[130:131]
	global_store_dwordx4 v2, v[132:135], s[34:35] offset:0 sc1
	global_store_dwordx4 v2, v[136:139], s[34:35] offset:1024 sc1
	global_store_dwordx4 v2, v[140:143], s[34:35] offset:2048 sc1
	global_store_dwordx4 v2, v[144:147], s[34:35] offset:3072 sc1
	s_waitcnt vmcnt(34)
	v_add_f32_dpp v112, v50, v50 quad_perm:[1,0,3,2] row_mask:0xf bank_mask:0xf
	s_mov_b64 s[36:37], s[24:25]
	s_add_u32 s24, s24, s22
	v_add_f32_dpp v112, v112, v112 quad_perm:[2,3,0,1] row_mask:0xf bank_mask:0xf
	s_addc_u32 s25, s25, 0
	s_nop 0
	v_add_f32_dpp v112, v112, v112 row_half_mirror row_mask:0xf bank_mask:0xf
	s_nop 1
	v_add_f32_dpp v112, v112, v112 row_mirror row_mask:0xf bank_mask:0xf
	v_fmamk_f32 v112, v112, 0x3a800000, v5
	v_rsq_f32_e32 v114, v112
	v_lshlrev_b32_e32 v116, 16, v42
	v_and_b32_e32 v117, 0xffff0000, v42
	v_lshlrev_b32_e32 v118, 16, v43
	v_and_b32_e32 v119, 0xffff0000, v43
	v_lshlrev_b32_e32 v120, 16, v44
	v_and_b32_e32 v121, 0xffff0000, v44
	v_lshlrev_b32_e32 v122, 16, v45
	v_and_b32_e32 v123, 0xffff0000, v45
	v_lshlrev_b32_e32 v124, 16, v46
	v_and_b32_e32 v125, 0xffff0000, v46
	v_lshlrev_b32_e32 v126, 16, v47
	v_and_b32_e32 v127, 0xffff0000, v47
	v_lshlrev_b32_e32 v128, 16, v48
	v_and_b32_e32 v129, 0xffff0000, v48
	v_lshlrev_b32_e32 v130, 16, v49
	v_and_b32_e32 v131, 0xffff0000, v49
	v_pk_mul_f32 v[116:117], v[114:115], v[116:117] op_sel_hi:[0,1]
	v_pk_mul_f32 v[118:119], v[114:115], v[118:119] op_sel_hi:[0,1]
	v_pk_mul_f32 v[120:121], v[114:115], v[120:121] op_sel_hi:[0,1]
	v_pk_mul_f32 v[122:123], v[114:115], v[122:123] op_sel_hi:[0,1]
	v_pk_mul_f32 v[124:125], v[114:115], v[124:125] op_sel_hi:[0,1]
	v_pk_mul_f32 v[126:127], v[114:115], v[126:127] op_sel_hi:[0,1]
	v_pk_mul_f32 v[128:129], v[114:115], v[128:129] op_sel_hi:[0,1]
	v_pk_mul_f32 v[130:131], v[114:115], v[130:131] op_sel_hi:[0,1]
	v_pk_mul_f32 v[132:133], v[8:9], v[116:117]
	v_pk_mul_f32 v[134:135], v[10:11], v[118:119]
	v_pk_mul_f32 v[136:137], v[12:13], v[120:121]
	v_pk_mul_f32 v[138:139], v[14:15], v[122:123]
	v_pk_mul_f32 v[140:141], v[16:17], v[124:125]
	v_pk_mul_f32 v[142:143], v[18:19], v[126:127]
	v_pk_mul_f32 v[144:145], v[20:21], v[128:129]
	v_pk_mul_f32 v[146:147], v[22:23], v[130:131]
	global_store_dwordx4 v2, v[132:135], s[36:37] offset:0 sc1
	global_store_dwordx4 v2, v[136:139], s[36:37] offset:1024 sc1
	global_store_dwordx4 v2, v[140:143], s[36:37] offset:2048 sc1
	global_store_dwordx4 v2, v[144:147], s[36:37] offset:3072 sc1
	s_waitcnt vmcnt(33)
	v_add_f32_dpp v112, v60, v60 quad_perm:[1,0,3,2] row_mask:0xf bank_mask:0xf
	s_mov_b64 s[34:35], s[24:25]
	s_add_u32 s24, s24, s22
	v_add_f32_dpp v112, v112, v112 quad_perm:[2,3,0,1] row_mask:0xf bank_mask:0xf
	s_addc_u32 s25, s25, 0
	s_nop 0
	v_add_f32_dpp v112, v112, v112 row_half_mirror row_mask:0xf bank_mask:0xf
	s_nop 1
	v_add_f32_dpp v112, v112, v112 row_mirror row_mask:0xf bank_mask:0xf
	v_fmamk_f32 v112, v112, 0x3a800000, v5
	v_rsq_f32_e32 v114, v112
	v_lshlrev_b32_e32 v116, 16, v52
	v_and_b32_e32 v117, 0xffff0000, v52
	v_lshlrev_b32_e32 v118, 16, v53
	v_and_b32_e32 v119, 0xffff0000, v53
	v_lshlrev_b32_e32 v120, 16, v54
	v_and_b32_e32 v121, 0xffff0000, v54
	v_lshlrev_b32_e32 v122, 16, v55
	v_and_b32_e32 v123, 0xffff0000, v55
	v_lshlrev_b32_e32 v124, 16, v56
	v_and_b32_e32 v125, 0xffff0000, v56
	v_lshlrev_b32_e32 v126, 16, v57
	v_and_b32_e32 v127, 0xffff0000, v57
	v_lshlrev_b32_e32 v128, 16, v58
	v_and_b32_e32 v129, 0xffff0000, v58
	v_lshlrev_b32_e32 v130, 16, v59
	v_and_b32_e32 v131, 0xffff0000, v59
	v_pk_mul_f32 v[116:117], v[114:115], v[116:117] op_sel_hi:[0,1]
	v_pk_mul_f32 v[118:119], v[114:115], v[118:119] op_sel_hi:[0,1]
	v_pk_mul_f32 v[120:121], v[114:115], v[120:121] op_sel_hi:[0,1]
	v_pk_mul_f32 v[122:123], v[114:115], v[122:123] op_sel_hi:[0,1]
	v_pk_mul_f32 v[124:125], v[114:115], v[124:125] op_sel_hi:[0,1]
	v_pk_mul_f32 v[126:127], v[114:115], v[126:127] op_sel_hi:[0,1]
	v_pk_mul_f32 v[128:129], v[114:115], v[128:129] op_sel_hi:[0,1]
	v_pk_mul_f32 v[130:131], v[114:115], v[130:131] op_sel_hi:[0,1]
	v_pk_mul_f32 v[132:133], v[8:9], v[116:117]
	v_pk_mul_f32 v[134:135], v[10:11], v[118:119]
	v_pk_mul_f32 v[136:137], v[12:13], v[120:121]
	v_pk_mul_f32 v[138:139], v[14:15], v[122:123]
	v_pk_mul_f32 v[140:141], v[16:17], v[124:125]
	v_pk_mul_f32 v[142:143], v[18:19], v[126:127]
	v_pk_mul_f32 v[144:145], v[20:21], v[128:129]
	v_pk_mul_f32 v[146:147], v[22:23], v[130:131]
	global_store_dwordx4 v2, v[132:135], s[34:35] offset:0 sc1
	global_store_dwordx4 v2, v[136:139], s[34:35] offset:1024 sc1
	global_store_dwordx4 v2, v[140:143], s[34:35] offset:2048 sc1
	global_store_dwordx4 v2, v[144:147], s[34:35] offset:3072 sc1
	s_waitcnt vmcnt(32)
	v_add_f32_dpp v112, v70, v70 quad_perm:[1,0,3,2] row_mask:0xf bank_mask:0xf
	s_mov_b64 s[36:37], s[24:25]
	s_add_u32 s24, s24, s22
	v_add_f32_dpp v112, v112, v112 quad_perm:[2,3,0,1] row_mask:0xf bank_mask:0xf
	s_addc_u32 s25, s25, 0
	s_nop 0
	v_add_f32_dpp v112, v112, v112 row_half_mirror row_mask:0xf bank_mask:0xf
	s_nop 1
	v_add_f32_dpp v112, v112, v112 row_mirror row_mask:0xf bank_mask:0xf
	v_fmamk_f32 v112, v112, 0x3a800000, v5
	v_rsq_f32_e32 v114, v112
	v_lshlrev_b32_e32 v116, 16, v62
	v_and_b32_e32 v117, 0xffff0000, v62
	v_lshlrev_b32_e32 v118, 16, v63
	v_and_b32_e32 v119, 0xffff0000, v63
	v_lshlrev_b32_e32 v120, 16, v64
	v_and_b32_e32 v121, 0xffff0000, v64
	v_lshlrev_b32_e32 v122, 16, v65
	v_and_b32_e32 v123, 0xffff0000, v65
	v_lshlrev_b32_e32 v124, 16, v66
	v_and_b32_e32 v125, 0xffff0000, v66
	v_lshlrev_b32_e32 v126, 16, v67
	v_and_b32_e32 v127, 0xffff0000, v67
	v_lshlrev_b32_e32 v128, 16, v68
	v_and_b32_e32 v129, 0xffff0000, v68
	v_lshlrev_b32_e32 v130, 16, v69
	v_and_b32_e32 v131, 0xffff0000, v69
	v_pk_mul_f32 v[116:117], v[114:115], v[116:117] op_sel_hi:[0,1]
	v_pk_mul_f32 v[118:119], v[114:115], v[118:119] op_sel_hi:[0,1]
	v_pk_mul_f32 v[120:121], v[114:115], v[120:121] op_sel_hi:[0,1]
	v_pk_mul_f32 v[122:123], v[114:115], v[122:123] op_sel_hi:[0,1]
	v_pk_mul_f32 v[124:125], v[114:115], v[124:125] op_sel_hi:[0,1]
	v_pk_mul_f32 v[126:127], v[114:115], v[126:127] op_sel_hi:[0,1]
	v_pk_mul_f32 v[128:129], v[114:115], v[128:129] op_sel_hi:[0,1]
	v_pk_mul_f32 v[130:131], v[114:115], v[130:131] op_sel_hi:[0,1]
	v_pk_mul_f32 v[132:133], v[8:9], v[116:117]
	v_pk_mul_f32 v[134:135], v[10:11], v[118:119]
	v_pk_mul_f32 v[136:137], v[12:13], v[120:121]
	v_pk_mul_f32 v[138:139], v[14:15], v[122:123]
	v_pk_mul_f32 v[140:141], v[16:17], v[124:125]
	v_pk_mul_f32 v[142:143], v[18:19], v[126:127]
	v_pk_mul_f32 v[144:145], v[20:21], v[128:129]
	v_pk_mul_f32 v[146:147], v[22:23], v[130:131]
	global_store_dwordx4 v2, v[132:135], s[36:37] offset:0 sc1
	global_store_dwordx4 v2, v[136:139], s[36:37] offset:1024 sc1
	global_store_dwordx4 v2, v[140:143], s[36:37] offset:2048 sc1
	global_store_dwordx4 v2, v[144:147], s[36:37] offset:3072 sc1
.Lfin_loop:
	s_add_i32 s14, s12, s23
	s_cmp_lt_i32 s14, 0x10000
	s_cbranch_scc0 .Lfin_drain
	s_mov_b64 s[26:27], s[16:17]
	s_mov_b64 s[28:29], s[18:19]
	global_load_dword v40, v4, s[26:27]
	global_load_dwordx2 v[32:33], v3, s[28:29] offset:0
	global_load_dwordx2 v[34:35], v3, s[28:29] offset:512
	global_load_dwordx2 v[36:37], v3, s[28:29] offset:1024
	global_load_dwordx2 v[38:39], v3, s[28:29] offset:1536
	s_add_u32 s16, s16, s20
	s_addc_u32 s17, s17, 0
	s_add_u32 s18, s18, s21
	s_addc_u32 s19, s19, 0
	s_add_i32 s12, s12, s13
	s_mov_b64 s[30:31], s[16:17]
	s_mov_b64 s[32:33], s[18:19]
	global_load_dword v50, v4, s[30:31]
	global_load_dwordx2 v[42:43], v3, s[32:33] offset:0
	global_load_dwordx2 v[44:45], v3, s[32:33] offset:512
	global_load_dwordx2 v[46:47], v3, s[32:33] offset:1024
	global_load_dwordx2 v[48:49], v3, s[32:33] offset:1536
	s_add_u32 s16, s16, s20
	s_addc_u32 s17, s17, 0
	s_add_u32 s18, s18, s21
	s_addc_u32 s19, s19, 0
	s_add_i32 s12, s12, s13
	s_mov_b64 s[26:27], s[16:17]
	s_mov_b64 s[28:29], s[18:19]
	global_load_dword v60, v4, s[26:27]
	global_load_dwordx2 v[52:53], v3, s[28:29] offset:0
	global_load_dwordx2 v[54:55], v3, s[28:29] offset:512
	global_load_dwordx2 v[56:57], v3, s[28:29] offset:1024
	global_load_dwordx2 v[58:59], v3, s[28:29] offset:1536
	s_add_u32 s16, s16, s20
	s_addc_u32 s17, s17, 0
	s_add_u32 s18, s18, s21
	s_addc_u32 s19, s19, 0
	s_add_i32 s12, s12, s13
	s_mov_b64 s[30:31], s[16:17]
	s_mov_b64 s[32:33], s[18:19]
	global_load_dword v70, v4, s[30:31]
	global_load_dwordx2 v[62:63], v3, s[32:33] offset:0
	global_load_dwordx2 v[64:65], v3, s[32:33] offset:512
	global_load_dwordx2 v[66:67], v3, s[32:33] offset:1024
	global_load_dwordx2 v[68:69], v3, s[32:33] offset:1536
	s_add_u32 s16, s16, s20
	s_addc_u32 s17, s17, 0
	s_add_u32 s18, s18, s21
	s_addc_u32 s19, s19, 0
	s_add_i32 s12, s12, s13
	s_waitcnt vmcnt(51)
	v_add_f32_dpp v112, v80, v80 quad_perm:[1,0,3,2] row_mask:0xf bank_mask:0xf
	s_mov_b64 s[34:35], s[24:25]
	s_add_u32 s24, s24, s22
	v_add_f32_dpp v112, v112, v112 quad_perm:[2,3,0,1] row_mask:0xf bank_mask:0xf
	s_addc_u32 s25, s25, 0
	s_nop 0
	v_add_f32_dpp v112, v112, v112 row_half_mirror row_mask:0xf bank_mask:0xf
	s_nop 1
	v_add_f32_dpp v112, v112, v112 row_mirror row_mask:0xf bank_mask:0xf
	v_fmamk_f32 v112, v112, 0x3a800000, v5
	v_rsq_f32_e32 v114, v112
	v_lshlrev_b32_e32 v116, 16, v72
	v_and_b32_e32 v117, 0xffff0000, v72
	v_lshlrev_b32_e32 v118, 16, v73
	v_and_b32_e32 v119, 0xffff0000, v73
	v_lshlrev_b32_e32 v120, 16, v74
	v_and_b32_e32 v121, 0xffff0000, v74
	v_lshlrev_b32_e32 v122, 16, v75
	v_and_b32_e32 v123, 0xffff0000, v75
	v_lshlrev_b32_e32 v124, 16, v76
	v_and_b32_e32 v125, 0xffff0000, v76
	v_lshlrev_b32_e32 v126, 16, v77
	v_and_b32_e32 v127, 0xffff0000, v77
	v_lshlrev_b32_e32 v128, 16, v78
	v_and_b32_e32 v129, 0xffff0000, v78
	v_lshlrev_b32_e32 v130, 16, v79
	v_and_b32_e32 v131, 0xffff0000, v79
	v_pk_mul_f32 v[116:117], v[114:115], v[116:117] op_sel_hi:[0,1]
	v_pk_mul_f32 v[118:119], v[114:115], v[118:119] op_sel_hi:[0,1]
	v_pk_mul_f32 v[120:121], v[114:115], v[120:121] op_sel_hi:[0,1]
	v_pk_mul_f32 v[122:123], v[114:115], v[122:123] op_sel_hi:[0,1]
	v_pk_mul_f32 v[124:125], v[114:115], v[124:125] op_sel_hi:[0,1]
	v_pk_mul_f32 v[126:127], v[114:115], v[126:127] op_sel_hi:[0,1]
	v_pk_mul_f32 v[128:129], v[114:115], v[128:129] op_sel_hi:[0,1]
	v_pk_mul_f32 v[130:131], v[114:115], v[130:131] op_sel_hi:[0,1]
	v_pk_mul_f32 v[132:133], v[8:9], v[116:117]
	v_pk_mul_f32 v[134:135], v[10:11], v[118:119]
	v_pk_mul_f32 v[136:137], v[12:13], v[120:121]
	v_pk_mul_f32 v[138:139], v[14:15], v[122:123]
	v_pk_mul_f32 v[140:141], v[16:17], v[124:125]
	v_pk_mul_f32 v[142:143], v[18:19], v[126:127]
	v_pk_mul_f32 v[144:145], v[20:21], v[128:129]
	v_pk_mul_f32 v[146:147], v[22:23], v[130:131]
	global_store_dwordx4 v2, v[132:135], s[34:35] offset:0 sc1
	global_store_dwordx4 v2, v[136:139], s[34:35] offset:1024 sc1
	global_store_dwordx4 v2, v[140:143], s[34:35] offset:2048 sc1
	global_store_dwordx4 v2, v[144:147], s[34:35] offset:3072 sc1
	s_waitcnt vmcnt(50)
	v_add_f32_dpp v112, v90, v90 quad_perm:[1,0,3,2] row_mask:0xf bank_mask:0xf
	s_mov_b64 s[36:37], s[24:25]
	s_add_u32 s24, s24, s22
	v_add_f32_dpp v112, v112, v112 quad_perm:[2,3,0,1] row_mask:0xf bank_mask:0xf
	s_addc_u32 s25, s25, 0
	s_nop 0
	v_add_f32_dpp v112, v112, v112 row_half_mirror row_mask:0xf bank_mask:0xf
	s_nop 1
	v_add_f32_dpp v112, v112, v112 row_mirror row_mask:0xf bank_mask:0xf
	v_fmamk_f32 v112, v112, 0x3a800000, v5
	v_rsq_f32_e32 v114, v112
	v_lshlrev_b32_e32 v116, 16, v82
	v_and_b32_e32 v117, 0xffff0000, v82
	v_lshlrev_b32_e32 v118, 16, v83
	v_and_b32_e32 v119, 0xffff0000, v83
	v_lshlrev_b32_e32 v120, 16, v84
	v_and_b32_e32 v121, 0xffff0000, v84
	v_lshlrev_b32_e32 v122, 16, v85
	v_and_b32_e32 v123, 0xffff0000, v85
	v_lshlrev_b32_e32 v124, 16, v86
	v_and_b32_e32 v125, 0xffff0000, v86
	v_lshlrev_b32_e32 v126, 16, v87
	v_and_b32_e32 v127, 0xffff0000, v87
	v_lshlrev_b32_e32 v128, 16, v88
	v_and_b32_e32 v129, 0xffff0000, v88
	v_lshlrev_b32_e32 v130, 16, v89
	v_and_b32_e32 v131, 0xffff0000, v89
	v_pk_mul_f32 v[116:117], v[114:115], v[116:117] op_sel_hi:[0,1]
	v_pk_mul_f32 v[118:119], v[114:115], v[118:119] op_sel_hi:[0,1]
	v_pk_mul_f32 v[120:121], v[114:115], v[120:121] op_sel_hi:[0,1]
	v_pk_mul_f32 v[122:123], v[114:115], v[122:123] op_sel_hi:[0,1]
	v_pk_mul_f32 v[124:125], v[114:115], v[124:125] op_sel_hi:[0,1]
	v_pk_mul_f32 v[126:127], v[114:115], v[126:127] op_sel_hi:[0,1]
	v_pk_mul_f32 v[128:129], v[114:115], v[128:129] op_sel_hi:[0,1]
	v_pk_mul_f32 v[130:131], v[114:115], v[130:131] op_sel_hi:[0,1]
	v_pk_mul_f32 v[132:133], v[8:9], v[116:117]
	v_pk_mul_f32 v[134:135], v[10:11], v[118:119]
	v_pk_mul_f32 v[136:137], v[12:13], v[120:121]
	v_pk_mul_f32 v[138:139], v[14:15], v[122:123]
	v_pk_mul_f32 v[140:141], v[16:17], v[124:125]
	v_pk_mul_f32 v[142:143], v[18:19], v[126:127]
	v_pk_mul_f32 v[144:145], v[20:21], v[128:129]
	v_pk_mul_f32 v[146:147], v[22:23], v[130:131]
	global_store_dwordx4 v2, v[132:135], s[36:37] offset:0 sc1
	global_store_dwordx4 v2, v[136:139], s[36:37] offset:1024 sc1
	global_store_dwordx4 v2, v[140:143], s[36:37] offset:2048 sc1
	global_store_dwordx4 v2, v[144:147], s[36:37] offset:3072 sc1
	s_waitcnt vmcnt(49)
	v_add_f32_dpp v112, v100, v100 quad_perm:[1,0,3,2] row_mask:0xf bank_mask:0xf
	s_mov_b64 s[34:35], s[24:25]
	s_add_u32 s24, s24, s22
	v_add_f32_dpp v112, v112, v112 quad_perm:[2,3,0,1] row_mask:0xf bank_mask:0xf
	s_addc_u32 s25, s25, 0
	s_nop 0
	v_add_f32_dpp v112, v112, v112 row_half_mirror row_mask:0xf bank_mask:0xf
	s_nop 1
	v_add_f32_dpp v112, v112, v112 row_mirror row_mask:0xf bank_mask:0xf
	v_fmamk_f32 v112, v112, 0x3a800000, v5
	v_rsq_f32_e32 v114, v112
	v_lshlrev_b32_e32 v116, 16, v92
	v_and_b32_e32 v117, 0xffff0000, v92
	v_lshlrev_b32_e32 v118, 16, v93
	v_and_b32_e32 v119, 0xffff0000, v93
	v_lshlrev_b32_e32 v120, 16, v94
	v_and_b32_e32 v121, 0xffff0000, v94
	v_lshlrev_b32_e32 v122, 16, v95
	v_and_b32_e32 v123, 0xffff0000, v95
	v_lshlrev_b32_e32 v124, 16, v96
	v_and_b32_e32 v125, 0xffff0000, v96
	v_lshlrev_b32_e32 v126, 16, v97
	v_and_b32_e32 v127, 0xffff0000, v97
	v_lshlrev_b32_e32 v128, 16, v98
	v_and_b32_e32 v129, 0xffff0000, v98
	v_lshlrev_b32_e32 v130, 16, v99
	v_and_b32_e32 v131, 0xffff0000, v99
	v_pk_mul_f32 v[116:117], v[114:115], v[116:117] op_sel_hi:[0,1]
	v_pk_mul_f32 v[118:119], v[114:115], v[118:119] op_sel_hi:[0,1]
	v_pk_mul_f32 v[120:121], v[114:115], v[120:121] op_sel_hi:[0,1]
	v_pk_mul_f32 v[122:123], v[114:115], v[122:123] op_sel_hi:[0,1]
	v_pk_mul_f32 v[124:125], v[114:115], v[124:125] op_sel_hi:[0,1]
	v_pk_mul_f32 v[126:127], v[114:115], v[126:127] op_sel_hi:[0,1]
	v_pk_mul_f32 v[128:129], v[114:115], v[128:129] op_sel_hi:[0,1]
	v_pk_mul_f32 v[130:131], v[114:115], v[130:131] op_sel_hi:[0,1]
	v_pk_mul_f32 v[132:133], v[8:9], v[116:117]
	v_pk_mul_f32 v[134:135], v[10:11], v[118:119]
	v_pk_mul_f32 v[136:137], v[12:13], v[120:121]
	v_pk_mul_f32 v[138:139], v[14:15], v[122:123]
	v_pk_mul_f32 v[140:141], v[16:17], v[124:125]
	v_pk_mul_f32 v[142:143], v[18:19], v[126:127]
	v_pk_mul_f32 v[144:145], v[20:21], v[128:129]
	v_pk_mul_f32 v[146:147], v[22:23], v[130:131]
	global_store_dwordx4 v2, v[132:135], s[34:35] offset:0 sc1
	global_store_dwordx4 v2, v[136:139], s[34:35] offset:1024 sc1
	global_store_dwordx4 v2, v[140:143], s[34:35] offset:2048 sc1
	global_store_dwordx4 v2, v[144:147], s[34:35] offset:3072 sc1
	s_waitcnt vmcnt(48)
	v_add_f32_dpp v112, v110, v110 quad_perm:[1,0,3,2] row_mask:0xf bank_mask:0xf
	s_mov_b64 s[36:37], s[24:25]
	s_add_u32 s24, s24, s22
	v_add_f32_dpp v112, v112, v112 quad_perm:[2,3,0,1] row_mask:0xf bank_mask:0xf
	s_addc_u32 s25, s25, 0
	s_nop 0
	v_add_f32_dpp v112, v112, v112 row_half_mirror row_mask:0xf bank_mask:0xf
	s_nop 1
	v_add_f32_dpp v112, v112, v112 row_mirror row_mask:0xf bank_mask:0xf
	v_fmamk_f32 v112, v112, 0x3a800000, v5
	v_rsq_f32_e32 v114, v112
	v_lshlrev_b32_e32 v116, 16, v102
	v_and_b32_e32 v117, 0xffff0000, v102
	v_lshlrev_b32_e32 v118, 16, v103
	v_and_b32_e32 v119, 0xffff0000, v103
	v_lshlrev_b32_e32 v120, 16, v104
	v_and_b32_e32 v121, 0xffff0000, v104
	v_lshlrev_b32_e32 v122, 16, v105
	v_and_b32_e32 v123, 0xffff0000, v105
	v_lshlrev_b32_e32 v124, 16, v106
	v_and_b32_e32 v125, 0xffff0000, v106
	v_lshlrev_b32_e32 v126, 16, v107
	v_and_b32_e32 v127, 0xffff0000, v107
	v_lshlrev_b32_e32 v128, 16, v108
	v_and_b32_e32 v129, 0xffff0000, v108
	v_lshlrev_b32_e32 v130, 16, v109
	v_and_b32_e32 v131, 0xffff0000, v109
	v_pk_mul_f32 v[116:117], v[114:115], v[116:117] op_sel_hi:[0,1]
	v_pk_mul_f32 v[118:119], v[114:115], v[118:119] op_sel_hi:[0,1]
	v_pk_mul_f32 v[120:121], v[114:115], v[120:121] op_sel_hi:[0,1]
	v_pk_mul_f32 v[122:123], v[114:115], v[122:123] op_sel_hi:[0,1]
	v_pk_mul_f32 v[124:125], v[114:115], v[124:125] op_sel_hi:[0,1]
	v_pk_mul_f32 v[126:127], v[114:115], v[126:127] op_sel_hi:[0,1]
	v_pk_mul_f32 v[128:129], v[114:115], v[128:129] op_sel_hi:[0,1]
	v_pk_mul_f32 v[130:131], v[114:115], v[130:131] op_sel_hi:[0,1]
	v_pk_mul_f32 v[132:133], v[8:9], v[116:117]
	v_pk_mul_f32 v[134:135], v[10:11], v[118:119]
	v_pk_mul_f32 v[136:137], v[12:13], v[120:121]
	v_pk_mul_f32 v[138:139], v[14:15], v[122:123]
	v_pk_mul_f32 v[140:141], v[16:17], v[124:125]
	v_pk_mul_f32 v[142:143], v[18:19], v[126:127]
	v_pk_mul_f32 v[144:145], v[20:21], v[128:129]
	v_pk_mul_f32 v[146:147], v[22:23], v[130:131]
	global_store_dwordx4 v2, v[132:135], s[36:37] offset:0 sc1
	global_store_dwordx4 v2, v[136:139], s[36:37] offset:1024 sc1
	global_store_dwordx4 v2, v[140:143], s[36:37] offset:2048 sc1
	global_store_dwordx4 v2, v[144:147], s[36:37] offset:3072 sc1
	s_mov_b64 s[26:27], s[16:17]
	s_mov_b64 s[28:29], s[18:19]
	global_load_dword v80, v4, s[26:27]
	global_load_dwordx2 v[72:73], v3, s[28:29] offset:0
	global_load_dwordx2 v[74:75], v3, s[28:29] offset:512
	global_load_dwordx2 v[76:77], v3, s[28:29] offset:1024
	global_load_dwordx2 v[78:79], v3, s[28:29] offset:1536
	s_add_u32 s16, s16, s20
	s_addc_u32 s17, s17, 0
	s_add_u32 s18, s18, s21
	s_addc_u32 s19, s19, 0
	s_add_i32 s12, s12, s13
	s_mov_b64 s[30:31], s[16:17]
	s_mov_b64 s[32:33], s[18:19]
	global_load_dword v90, v4, s[30:31]
	global_load_dwordx2 v[82:83], v3, s[32:33] offset:0
	global_load_dwordx2 v[84:85], v3, s[32:33] offset:512
	global_load_dwordx2 v[86:87], v3, s[32:33] offset:1024
	global_load_dwordx2 v[88:89], v3, s[32:33] offset:1536
	s_add_u32 s16, s16, s20
	s_addc_u32 s17, s17, 0
	s_add_u32 s18, s18, s21
	s_addc_u32 s19, s19, 0
	s_add_i32 s12, s12, s13
	s_mov_b64 s[26:27], s[16:17]
	s_mov_b64 s[28:29], s[18:19]
	global_load_dword v100, v4, s[26:27]
	global_load_dwordx2 v[92:93], v3, s[28:29] offset:0
	global_load_dwordx2 v[94:95], v3, s[28:29] offset:512
	global_load_dwordx2 v[96:97], v3, s[28:29] offset:1024
	global_load_dwordx2 v[98:99], v3, s[28:29] offset:1536
	s_add_u32 s16, s16, s20
	s_addc_u32 s17, s17, 0
	s_add_u32 s18, s18, s21
	s_addc_u32 s19, s19, 0
	s_add_i32 s12, s12, s13
	s_mov_b64 s[30:31], s[16:17]
	s_mov_b64 s[32:33], s[18:19]
	global_load_dword v110, v4, s[30:31]
	global_load_dwordx2 v[102:103], v3, s[32:33] offset:0
	global_load_dwordx2 v[104:105], v3, s[32:33] offset:512
	global_load_dwordx2 v[106:107], v3, s[32:33] offset:1024
	global_load_dwordx2 v[108:109], v3, s[32:33] offset:1536
	s_add_u32 s16, s16, s20
	s_addc_u32 s17, s17, 0
	s_add_u32 s18, s18, s21
	s_addc_u32 s19, s19, 0
	s_add_i32 s12, s12, s13
	s_waitcnt vmcnt(51)
	v_add_f32_dpp v112, v40, v40 quad_perm:[1,0,3,2] row_mask:0xf bank_mask:0xf
	s_mov_b64 s[34:35], s[24:25]
	s_add_u32 s24, s24, s22
	v_add_f32_dpp v112, v112, v112 quad_perm:[2,3,0,1] row_mask:0xf bank_mask:0xf
	s_addc_u32 s25, s25, 0
	s_nop 0
	v_add_f32_dpp v112, v112, v112 row_half_mirror row_mask:0xf bank_mask:0xf
	s_nop 1
	v_add_f32_dpp v112, v112, v112 row_mirror row_mask:0xf bank_mask:0xf
	v_fmamk_f32 v112, v112, 0x3a800000, v5
	v_rsq_f32_e32 v114, v112
	v_lshlrev_b32_e32 v116, 16, v32
	v_and_b32_e32 v117, 0xffff0000, v32
	v_lshlrev_b32_e32 v118, 16, v33
	v_and_b32_e32 v119, 0xffff0000, v33
	v_lshlrev_b32_e32 v120, 16, v34
	v_and_b32_e32 v121, 0xffff0000, v34
	v_lshlrev_b32_e32 v122, 16, v35
	v_and_b32_e32 v123, 0xffff0000, v35
	v_lshlrev_b32_e32 v124, 16, v36
	v_and_b32_e32 v125, 0xffff0000, v36
	v_lshlrev_b32_e32 v126, 16, v37
	v_and_b32_e32 v127, 0xffff0000, v37
	v_lshlrev_b32_e32 v128, 16, v38
	v_and_b32_e32 v129, 0xffff0000, v38
	v_lshlrev_b32_e32 v130, 16, v39
	v_and_b32_e32 v131, 0xffff0000, v39
	v_pk_mul_f32 v[116:117], v[114:115], v[116:117] op_sel_hi:[0,1]
	v_pk_mul_f32 v[118:119], v[114:115], v[118:119] op_sel_hi:[0,1]
	v_pk_mul_f32 v[120:121], v[114:115], v[120:121] op_sel_hi:[0,1]
	v_pk_mul_f32 v[122:123], v[114:115], v[122:123] op_sel_hi:[0,1]
	v_pk_mul_f32 v[124:125], v[114:115], v[124:125] op_sel_hi:[0,1]
	v_pk_mul_f32 v[126:127], v[114:115], v[126:127] op_sel_hi:[0,1]
	v_pk_mul_f32 v[128:129], v[114:115], v[128:129] op_sel_hi:[0,1]
	v_pk_mul_f32 v[130:131], v[114:115], v[130:131] op_sel_hi:[0,1]
	v_pk_mul_f32 v[132:133], v[8:9], v[116:117]
	v_pk_mul_f32 v[134:135], v[10:11], v[118:119]
	v_pk_mul_f32 v[136:137], v[12:13], v[120:121]
	v_pk_mul_f32 v[138:139], v[14:15], v[122:123]
	v_pk_mul_f32 v[140:141], v[16:17], v[124:125]
	v_pk_mul_f32 v[142:143], v[18:19], v[126:127]
	v_pk_mul_f32 v[144:145], v[20:21], v[128:129]
	v_pk_mul_f32 v[146:147], v[22:23], v[130:131]
	global_store_dwordx4 v2, v[132:135], s[34:35] offset:0 sc1
	global_store_dwordx4 v2, v[136:139], s[34:35] offset:1024 sc1
	global_store_dwordx4 v2, v[140:143], s[34:35] offset:2048 sc1
	global_store_dwordx4 v2, v[144:147], s[34:35] offset:3072 sc1
	s_waitcnt vmcnt(50)
	v_add_f32_dpp v112, v50, v50 quad_perm:[1,0,3,2] row_mask:0xf bank_mask:0xf
	s_mov_b64 s[36:37], s[24:25]
	s_add_u32 s24, s24, s22
	v_add_f32_dpp v112, v112, v112 quad_perm:[2,3,0,1] row_mask:0xf bank_mask:0xf
	s_addc_u32 s25, s25, 0
	s_nop 0
	v_add_f32_dpp v112, v112, v112 row_half_mirror row_mask:0xf bank_mask:0xf
	s_nop 1
	v_add_f32_dpp v112, v112, v112 row_mirror row_mask:0xf bank_mask:0xf
	v_fmamk_f32 v112, v112, 0x3a800000, v5
	v_rsq_f32_e32 v114, v112
	v_lshlrev_b32_e32 v116, 16, v42
	v_and_b32_e32 v117, 0xffff0000, v42
	v_lshlrev_b32_e32 v118, 16, v43
	v_and_b32_e32 v119, 0xffff0000, v43
	v_lshlrev_b32_e32 v120, 16, v44
	v_and_b32_e32 v121, 0xffff0000, v44
	v_lshlrev_b32_e32 v122, 16, v45
	v_and_b32_e32 v123, 0xffff0000, v45
	v_lshlrev_b32_e32 v124, 16, v46
	v_and_b32_e32 v125, 0xffff0000, v46
	v_lshlrev_b32_e32 v126, 16, v47
	v_and_b32_e32 v127, 0xffff0000, v47
	v_lshlrev_b32_e32 v128, 16, v48
	v_and_b32_e32 v129, 0xffff0000, v48
	v_lshlrev_b32_e32 v130, 16, v49
	v_and_b32_e32 v131, 0xffff0000, v49
	v_pk_mul_f32 v[116:117], v[114:115], v[116:117] op_sel_hi:[0,1]
	v_pk_mul_f32 v[118:119], v[114:115], v[118:119] op_sel_hi:[0,1]
	v_pk_mul_f32 v[120:121], v[114:115], v[120:121] op_sel_hi:[0,1]
	v_pk_mul_f32 v[122:123], v[114:115], v[122:123] op_sel_hi:[0,1]
	v_pk_mul_f32 v[124:125], v[114:115], v[124:125] op_sel_hi:[0,1]
	v_pk_mul_f32 v[126:127], v[114:115], v[126:127] op_sel_hi:[0,1]
	v_pk_mul_f32 v[128:129], v[114:115], v[128:129] op_sel_hi:[0,1]
	v_pk_mul_f32 v[130:131], v[114:115], v[130:131] op_sel_hi:[0,1]
	v_pk_mul_f32 v[132:133], v[8:9], v[116:117]
	v_pk_mul_f32 v[134:135], v[10:11], v[118:119]
	v_pk_mul_f32 v[136:137], v[12:13], v[120:121]
	v_pk_mul_f32 v[138:139], v[14:15], v[122:123]
	v_pk_mul_f32 v[140:141], v[16:17], v[124:125]
	v_pk_mul_f32 v[142:143], v[18:19], v[126:127]
	v_pk_mul_f32 v[144:145], v[20:21], v[128:129]
	v_pk_mul_f32 v[146:147], v[22:23], v[130:131]
	global_store_dwordx4 v2, v[132:135], s[36:37] offset:0 sc1
	global_store_dwordx4 v2, v[136:139], s[36:37] offset:1024 sc1
	global_store_dwordx4 v2, v[140:143], s[36:37] offset:2048 sc1
	global_store_dwordx4 v2, v[144:147], s[36:37] offset:3072 sc1
	s_waitcnt vmcnt(49)
	v_add_f32_dpp v112, v60, v60 quad_perm:[1,0,3,2] row_mask:0xf bank_mask:0xf
	s_mov_b64 s[34:35], s[24:25]
	s_add_u32 s24, s24, s22
	v_add_f32_dpp v112, v112, v112 quad_perm:[2,3,0,1] row_mask:0xf bank_mask:0xf
	s_addc_u32 s25, s25, 0
	s_nop 0
	v_add_f32_dpp v112, v112, v112 row_half_mirror row_mask:0xf bank_mask:0xf
	s_nop 1
	v_add_f32_dpp v112, v112, v112 row_mirror row_mask:0xf bank_mask:0xf
	v_fmamk_f32 v112, v112, 0x3a800000, v5
	v_rsq_f32_e32 v114, v112
	v_lshlrev_b32_e32 v116, 16, v52
	v_and_b32_e32 v117, 0xffff0000, v52
	v_lshlrev_b32_e32 v118, 16, v53
	v_and_b32_e32 v119, 0xffff0000, v53
	v_lshlrev_b32_e32 v120, 16, v54
	v_and_b32_e32 v121, 0xffff0000, v54
	v_lshlrev_b32_e32 v122, 16, v55
	v_and_b32_e32 v123, 0xffff0000, v55
	v_lshlrev_b32_e32 v124, 16, v56
	v_and_b32_e32 v125, 0xffff0000, v56
	v_lshlrev_b32_e32 v126, 16, v57
	v_and_b32_e32 v127, 0xffff0000, v57
	v_lshlrev_b32_e32 v128, 16, v58
	v_and_b32_e32 v129, 0xffff0000, v58
	v_lshlrev_b32_e32 v130, 16, v59
	v_and_b32_e32 v131, 0xffff0000, v59
	v_pk_mul_f32 v[116:117], v[114:115], v[116:117] op_sel_hi:[0,1]
	v_pk_mul_f32 v[118:119], v[114:115], v[118:119] op_sel_hi:[0,1]
	v_pk_mul_f32 v[120:121], v[114:115], v[120:121] op_sel_hi:[0,1]
	v_pk_mul_f32 v[122:123], v[114:115], v[122:123] op_sel_hi:[0,1]
	v_pk_mul_f32 v[124:125], v[114:115], v[124:125] op_sel_hi:[0,1]
	v_pk_mul_f32 v[126:127], v[114:115], v[126:127] op_sel_hi:[0,1]
	v_pk_mul_f32 v[128:129], v[114:115], v[128:129] op_sel_hi:[0,1]
	v_pk_mul_f32 v[130:131], v[114:115], v[130:131] op_sel_hi:[0,1]
	v_pk_mul_f32 v[132:133], v[8:9], v[116:117]
	v_pk_mul_f32 v[134:135], v[10:11], v[118:119]
	v_pk_mul_f32 v[136:137], v[12:13], v[120:121]
	v_pk_mul_f32 v[138:139], v[14:15], v[122:123]
	v_pk_mul_f32 v[140:141], v[16:17], v[124:125]
	v_pk_mul_f32 v[142:143], v[18:19], v[126:127]
	v_pk_mul_f32 v[144:145], v[20:21], v[128:129]
	v_pk_mul_f32 v[146:147], v[22:23], v[130:131]
	global_store_dwordx4 v2, v[132:135], s[34:35] offset:0 sc1
	global_store_dwordx4 v2, v[136:139], s[34:35] offset:1024 sc1
	global_store_dwordx4 v2, v[140:143], s[34:35] offset:2048 sc1
	global_store_dwordx4 v2, v[144:147], s[34:35] offset:3072 sc1
	s_waitcnt vmcnt(48)
	v_add_f32_dpp v112, v70, v70 quad_perm:[1,0,3,2] row_mask:0xf bank_mask:0xf
	s_mov_b64 s[36:37], s[24:25]
	s_add_u32 s24, s24, s22
	v_add_f32_dpp v112, v112, v112 quad_perm:[2,3,0,1] row_mask:0xf bank_mask:0xf
	s_addc_u32 s25, s25, 0
	s_nop 0
	v_add_f32_dpp v112, v112, v112 row_half_mirror row_mask:0xf bank_mask:0xf
	s_nop 1
	v_add_f32_dpp v112, v112, v112 row_mirror row_mask:0xf bank_mask:0xf
	v_fmamk_f32 v112, v112, 0x3a800000, v5
	v_rsq_f32_e32 v114, v112
	v_lshlrev_b32_e32 v116, 16, v62
	v_and_b32_e32 v117, 0xffff0000, v62
	v_lshlrev_b32_e32 v118, 16, v63
	v_and_b32_e32 v119, 0xffff0000, v63
	v_lshlrev_b32_e32 v120, 16, v64
	v_and_b32_e32 v121, 0xffff0000, v64
	v_lshlrev_b32_e32 v122, 16, v65
	v_and_b32_e32 v123, 0xffff0000, v65
	v_lshlrev_b32_e32 v124, 16, v66
	v_and_b32_e32 v125, 0xffff0000, v66
	v_lshlrev_b32_e32 v126, 16, v67
	v_and_b32_e32 v127, 0xffff0000, v67
	v_lshlrev_b32_e32 v128, 16, v68
	v_and_b32_e32 v129, 0xffff0000, v68
	v_lshlrev_b32_e32 v130, 16, v69
	v_and_b32_e32 v131, 0xffff0000, v69
	v_pk_mul_f32 v[116:117], v[114:115], v[116:117] op_sel_hi:[0,1]
	v_pk_mul_f32 v[118:119], v[114:115], v[118:119] op_sel_hi:[0,1]
	v_pk_mul_f32 v[120:121], v[114:115], v[120:121] op_sel_hi:[0,1]
	v_pk_mul_f32 v[122:123], v[114:115], v[122:123] op_sel_hi:[0,1]
	v_pk_mul_f32 v[124:125], v[114:115], v[124:125] op_sel_hi:[0,1]
	v_pk_mul_f32 v[126:127], v[114:115], v[126:127] op_sel_hi:[0,1]
	v_pk_mul_f32 v[128:129], v[114:115], v[128:129] op_sel_hi:[0,1]
	v_pk_mul_f32 v[130:131], v[114:115], v[130:131] op_sel_hi:[0,1]
	v_pk_mul_f32 v[132:133], v[8:9], v[116:117]
	v_pk_mul_f32 v[134:135], v[10:11], v[118:119]
	v_pk_mul_f32 v[136:137], v[12:13], v[120:121]
	v_pk_mul_f32 v[138:139], v[14:15], v[122:123]
	v_pk_mul_f32 v[140:141], v[16:17], v[124:125]
	v_pk_mul_f32 v[142:143], v[18:19], v[126:127]
	v_pk_mul_f32 v[144:145], v[20:21], v[128:129]
	v_pk_mul_f32 v[146:147], v[22:23], v[130:131]
	global_store_dwordx4 v2, v[132:135], s[36:37] offset:0 sc1
	global_store_dwordx4 v2, v[136:139], s[36:37] offset:1024 sc1
	global_store_dwordx4 v2, v[140:143], s[36:37] offset:2048 sc1
	global_store_dwordx4 v2, v[144:147], s[36:37] offset:3072 sc1
	s_branch .Lfin_loop
.Lfin_drain:
	s_waitcnt vmcnt(31)
	v_add_f32_dpp v112, v80, v80 quad_perm:[1,0,3,2] row_mask:0xf bank_mask:0xf
	s_mov_b64 s[34:35], s[24:25]
	s_add_u32 s24, s24, s22
	v_add_f32_dpp v112, v112, v112 quad_perm:[2,3,0,1] row_mask:0xf bank_mask:0xf
	s_addc_u32 s25, s25, 0
	s_nop 0
	v_add_f32_dpp v112, v112, v112 row_half_mirror row_mask:0xf bank_mask:0xf
	s_nop 1
	v_add_f32_dpp v112, v112, v112 row_mirror row_mask:0xf bank_mask:0xf
	v_fmamk_f32 v112, v112, 0x3a800000, v5
	v_rsq_f32_e32 v114, v112
	v_lshlrev_b32_e32 v116, 16, v72
	v_and_b32_e32 v117, 0xffff0000, v72
	v_lshlrev_b32_e32 v118, 16, v73
	v_and_b32_e32 v119, 0xffff0000, v73
	v_lshlrev_b32_e32 v120, 16, v74
	v_and_b32_e32 v121, 0xffff0000, v74
	v_lshlrev_b32_e32 v122, 16, v75
	v_and_b32_e32 v123, 0xffff0000, v75
	v_lshlrev_b32_e32 v124, 16, v76
	v_and_b32_e32 v125, 0xffff0000, v76
	v_lshlrev_b32_e32 v126, 16, v77
	v_and_b32_e32 v127, 0xffff0000, v77
	v_lshlrev_b32_e32 v128, 16, v78
	v_and_b32_e32 v129, 0xffff0000, v78
	v_lshlrev_b32_e32 v130, 16, v79
	v_and_b32_e32 v131, 0xffff0000, v79
	v_pk_mul_f32 v[116:117], v[114:115], v[116:117] op_sel_hi:[0,1]
	v_pk_mul_f32 v[118:119], v[114:115], v[118:119] op_sel_hi:[0,1]
	v_pk_mul_f32 v[120:121], v[114:115], v[120:121] op_sel_hi:[0,1]
	v_pk_mul_f32 v[122:123], v[114:115], v[122:123] op_sel_hi:[0,1]
	v_pk_mul_f32 v[124:125], v[114:115], v[124:125] op_sel_hi:[0,1]
	v_pk_mul_f32 v[126:127], v[114:115], v[126:127] op_sel_hi:[0,1]
	v_pk_mul_f32 v[128:129], v[114:115], v[128:129] op_sel_hi:[0,1]
	v_pk_mul_f32 v[130:131], v[114:115], v[130:131] op_sel_hi:[0,1]
	v_pk_mul_f32 v[132:133], v[8:9], v[116:117]
	v_pk_mul_f32 v[134:135], v[10:11], v[118:119]
	v_pk_mul_f32 v[136:137], v[12:13], v[120:121]
	v_pk_mul_f32 v[138:139], v[14:15], v[122:123]
	v_pk_mul_f32 v[140:141], v[16:17], v[124:125]
	v_pk_mul_f32 v[142:143], v[18:19], v[126:127]
	v_pk_mul_f32 v[144:145], v[20:21], v[128:129]
	v_pk_mul_f32 v[146:147], v[22:23], v[130:131]
	global_store_dwordx4 v2, v[132:135], s[34:35] offset:0 sc1
	global_store_dwordx4 v2, v[136:139], s[34:35] offset:1024 sc1
	global_store_dwordx4 v2, v[140:143], s[34:35] offset:2048 sc1
	global_store_dwordx4 v2, v[144:147], s[34:35] offset:3072 sc1
	s_waitcnt vmcnt(30)
	v_add_f32_dpp v112, v90, v90 quad_perm:[1,0,3,2] row_mask:0xf bank_mask:0xf
	s_mov_b64 s[36:37], s[24:25]
	s_add_u32 s24, s24, s22
	v_add_f32_dpp v112, v112, v112 quad_perm:[2,3,0,1] row_mask:0xf bank_mask:0xf
	s_addc_u32 s25, s25, 0
	s_nop 0
	v_add_f32_dpp v112, v112, v112 row_half_mirror row_mask:0xf bank_mask:0xf
	s_nop 1
	v_add_f32_dpp v112, v112, v112 row_mirror row_mask:0xf bank_mask:0xf
	v_fmamk_f32 v112, v112, 0x3a800000, v5
	v_rsq_f32_e32 v114, v112
	v_lshlrev_b32_e32 v116, 16, v82
	v_and_b32_e32 v117, 0xffff0000, v82
	v_lshlrev_b32_e32 v118, 16, v83
	v_and_b32_e32 v119, 0xffff0000, v83
	v_lshlrev_b32_e32 v120, 16, v84
	v_and_b32_e32 v121, 0xffff0000, v84
	v_lshlrev_b32_e32 v122, 16, v85
	v_and_b32_e32 v123, 0xffff0000, v85
	v_lshlrev_b32_e32 v124, 16, v86
	v_and_b32_e32 v125, 0xffff0000, v86
	v_lshlrev_b32_e32 v126, 16, v87
	v_and_b32_e32 v127, 0xffff0000, v87
	v_lshlrev_b32_e32 v128, 16, v88
	v_and_b32_e32 v129, 0xffff0000, v88
	v_lshlrev_b32_e32 v130, 16, v89
	v_and_b32_e32 v131, 0xffff0000, v89
	v_pk_mul_f32 v[116:117], v[114:115], v[116:117] op_sel_hi:[0,1]
	v_pk_mul_f32 v[118:119], v[114:115], v[118:119] op_sel_hi:[0,1]
	v_pk_mul_f32 v[120:121], v[114:115], v[120:121] op_sel_hi:[0,1]
	v_pk_mul_f32 v[122:123], v[114:115], v[122:123] op_sel_hi:[0,1]
	v_pk_mul_f32 v[124:125], v[114:115], v[124:125] op_sel_hi:[0,1]
	v_pk_mul_f32 v[126:127], v[114:115], v[126:127] op_sel_hi:[0,1]
	v_pk_mul_f32 v[128:129], v[114:115], v[128:129] op_sel_hi:[0,1]
	v_pk_mul_f32 v[130:131], v[114:115], v[130:131] op_sel_hi:[0,1]
	v_pk_mul_f32 v[132:133], v[8:9], v[116:117]
	v_pk_mul_f32 v[134:135], v[10:11], v[118:119]
	v_pk_mul_f32 v[136:137], v[12:13], v[120:121]
	v_pk_mul_f32 v[138:139], v[14:15], v[122:123]
	v_pk_mul_f32 v[140:141], v[16:17], v[124:125]
	v_pk_mul_f32 v[142:143], v[18:19], v[126:127]
	v_pk_mul_f32 v[144:145], v[20:21], v[128:129]
	v_pk_mul_f32 v[146:147], v[22:23], v[130:131]
	global_store_dwordx4 v2, v[132:135], s[36:37] offset:0 sc1
	global_store_dwordx4 v2, v[136:139], s[36:37] offset:1024 sc1
	global_store_dwordx4 v2, v[140:143], s[36:37] offset:2048 sc1
	global_store_dwordx4 v2, v[144:147], s[36:37] offset:3072 sc1
	s_waitcnt vmcnt(29)
	v_add_f32_dpp v112, v100, v100 quad_perm:[1,0,3,2] row_mask:0xf bank_mask:0xf
	s_mov_b64 s[34:35], s[24:25]
	s_add_u32 s24, s24, s22
	v_add_f32_dpp v112, v112, v112 quad_perm:[2,3,0,1] row_mask:0xf bank_mask:0xf
	s_addc_u32 s25, s25, 0
	s_nop 0
	v_add_f32_dpp v112, v112, v112 row_half_mirror row_mask:0xf bank_mask:0xf
	s_nop 1
	v_add_f32_dpp v112, v112, v112 row_mirror row_mask:0xf bank_mask:0xf
	v_fmamk_f32 v112, v112, 0x3a800000, v5
	v_rsq_f32_e32 v114, v112
	v_lshlrev_b32_e32 v116, 16, v92
	v_and_b32_e32 v117, 0xffff0000, v92
	v_lshlrev_b32_e32 v118, 16, v93
	v_and_b32_e32 v119, 0xffff0000, v93
	v_lshlrev_b32_e32 v120, 16, v94
	v_and_b32_e32 v121, 0xffff0000, v94
	v_lshlrev_b32_e32 v122, 16, v95
	v_and_b32_e32 v123, 0xffff0000, v95
	v_lshlrev_b32_e32 v124, 16, v96
	v_and_b32_e32 v125, 0xffff0000, v96
	v_lshlrev_b32_e32 v126, 16, v97
	v_and_b32_e32 v127, 0xffff0000, v97
	v_lshlrev_b32_e32 v128, 16, v98
	v_and_b32_e32 v129, 0xffff0000, v98
	v_lshlrev_b32_e32 v130, 16, v99
	v_and_b32_e32 v131, 0xffff0000, v99
	v_pk_mul_f32 v[116:117], v[114:115], v[116:117] op_sel_hi:[0,1]
	v_pk_mul_f32 v[118:119], v[114:115], v[118:119] op_sel_hi:[0,1]
	v_pk_mul_f32 v[120:121], v[114:115], v[120:121] op_sel_hi:[0,1]
	v_pk_mul_f32 v[122:123], v[114:115], v[122:123] op_sel_hi:[0,1]
	v_pk_mul_f32 v[124:125], v[114:115], v[124:125] op_sel_hi:[0,1]
	v_pk_mul_f32 v[126:127], v[114:115], v[126:127] op_sel_hi:[0,1]
	v_pk_mul_f32 v[128:129], v[114:115], v[128:129] op_sel_hi:[0,1]
	v_pk_mul_f32 v[130:131], v[114:115], v[130:131] op_sel_hi:[0,1]
	v_pk_mul_f32 v[132:133], v[8:9], v[116:117]
	v_pk_mul_f32 v[134:135], v[10:11], v[118:119]
	v_pk_mul_f32 v[136:137], v[12:13], v[120:121]
	v_pk_mul_f32 v[138:139], v[14:15], v[122:123]
	v_pk_mul_f32 v[140:141], v[16:17], v[124:125]
	v_pk_mul_f32 v[142:143], v[18:19], v[126:127]
	v_pk_mul_f32 v[144:145], v[20:21], v[128:129]
	v_pk_mul_f32 v[146:147], v[22:23], v[130:131]
	global_store_dwordx4 v2, v[132:135], s[34:35] offset:0 sc1
	global_store_dwordx4 v2, v[136:139], s[34:35] offset:1024 sc1
	global_store_dwordx4 v2, v[140:143], s[34:35] offset:2048 sc1
	global_store_dwordx4 v2, v[144:147], s[34:35] offset:3072 sc1
	s_waitcnt vmcnt(28)
	v_add_f32_dpp v112, v110, v110 quad_perm:[1,0,3,2] row_mask:0xf bank_mask:0xf
	s_mov_b64 s[36:37], s[24:25]
	s_add_u32 s24, s24, s22
	v_add_f32_dpp v112, v112, v112 quad_perm:[2,3,0,1] row_mask:0xf bank_mask:0xf
	s_addc_u32 s25, s25, 0
	s_nop 0
	v_add_f32_dpp v112, v112, v112 row_half_mirror row_mask:0xf bank_mask:0xf
	s_nop 1
	v_add_f32_dpp v112, v112, v112 row_mirror row_mask:0xf bank_mask:0xf
	v_fmamk_f32 v112, v112, 0x3a800000, v5
	v_rsq_f32_e32 v114, v112
	v_lshlrev_b32_e32 v116, 16, v102
	v_and_b32_e32 v117, 0xffff0000, v102
	v_lshlrev_b32_e32 v118, 16, v103
	v_and_b32_e32 v119, 0xffff0000, v103
	v_lshlrev_b32_e32 v120, 16, v104
	v_and_b32_e32 v121, 0xffff0000, v104
	v_lshlrev_b32_e32 v122, 16, v105
	v_and_b32_e32 v123, 0xffff0000, v105
	v_lshlrev_b32_e32 v124, 16, v106
	v_and_b32_e32 v125, 0xffff0000, v106
	v_lshlrev_b32_e32 v126, 16, v107
	v_and_b32_e32 v127, 0xffff0000, v107
	v_lshlrev_b32_e32 v128, 16, v108
	v_and_b32_e32 v129, 0xffff0000, v108
	v_lshlrev_b32_e32 v130, 16, v109
	v_and_b32_e32 v131, 0xffff0000, v109
	v_pk_mul_f32 v[116:117], v[114:115], v[116:117] op_sel_hi:[0,1]
	v_pk_mul_f32 v[118:119], v[114:115], v[118:119] op_sel_hi:[0,1]
	v_pk_mul_f32 v[120:121], v[114:115], v[120:121] op_sel_hi:[0,1]
	v_pk_mul_f32 v[122:123], v[114:115], v[122:123] op_sel_hi:[0,1]
	v_pk_mul_f32 v[124:125], v[114:115], v[124:125] op_sel_hi:[0,1]
	v_pk_mul_f32 v[126:127], v[114:115], v[126:127] op_sel_hi:[0,1]
	v_pk_mul_f32 v[128:129], v[114:115], v[128:129] op_sel_hi:[0,1]
	v_pk_mul_f32 v[130:131], v[114:115], v[130:131] op_sel_hi:[0,1]
	v_pk_mul_f32 v[132:133], v[8:9], v[116:117]
	v_pk_mul_f32 v[134:135], v[10:11], v[118:119]
	v_pk_mul_f32 v[136:137], v[12:13], v[120:121]
	v_pk_mul_f32 v[138:139], v[14:15], v[122:123]
	v_pk_mul_f32 v[140:141], v[16:17], v[124:125]
	v_pk_mul_f32 v[142:143], v[18:19], v[126:127]
	v_pk_mul_f32 v[144:145], v[20:21], v[128:129]
	v_pk_mul_f32 v[146:147], v[22:23], v[130:131]
	global_store_dwordx4 v2, v[132:135], s[36:37] offset:0 sc1
	global_store_dwordx4 v2, v[136:139], s[36:37] offset:1024 sc1
	global_store_dwordx4 v2, v[140:143], s[36:37] offset:2048 sc1
	global_store_dwordx4 v2, v[144:147], s[36:37] offset:3072 sc1
.Lfin_tail:
	s_cmp_lt_i32 s12, 0x10000
	s_cbranch_scc0 .LBB0_3641
	s_mov_b64 s[26:27], s[16:17]
	s_mov_b64 s[28:29], s[18:19]
	global_load_dword v40, v4, s[26:27]
	global_load_dwordx2 v[32:33], v3, s[28:29] offset:0
	global_load_dwordx2 v[34:35], v3, s[28:29] offset:512
	global_load_dwordx2 v[36:37], v3, s[28:29] offset:1024
	global_load_dwordx2 v[38:39], v3, s[28:29] offset:1536
	s_add_u32 s16, s16, s20
	s_addc_u32 s17, s17, 0
	s_add_u32 s18, s18, s21
	s_addc_u32 s19, s19, 0
	s_add_i32 s12, s12, s13
	s_waitcnt vmcnt(0)
	v_add_f32_dpp v112, v40, v40 quad_perm:[1,0,3,2] row_mask:0xf bank_mask:0xf
	s_mov_b64 s[34:35], s[24:25]
	s_add_u32 s24, s24, s22
	v_add_f32_dpp v112, v112, v112 quad_perm:[2,3,0,1] row_mask:0xf bank_mask:0xf
	s_addc_u32 s25, s25, 0
	s_nop 0
	v_add_f32_dpp v112, v112, v112 row_half_mirror row_mask:0xf bank_mask:0xf
	s_nop 1
	v_add_f32_dpp v112, v112, v112 row_mirror row_mask:0xf bank_mask:0xf
	v_fmamk_f32 v112, v112, 0x3a800000, v5
	v_rsq_f32_e32 v114, v112
	v_lshlrev_b32_e32 v116, 16, v32
	v_and_b32_e32 v117, 0xffff0000, v32
	v_lshlrev_b32_e32 v118, 16, v33
	v_and_b32_e32 v119, 0xffff0000, v33
	v_lshlrev_b32_e32 v120, 16, v34
	v_and_b32_e32 v121, 0xffff0000, v34
	v_lshlrev_b32_e32 v122, 16, v35
	v_and_b32_e32 v123, 0xffff0000, v35
	v_lshlrev_b32_e32 v124, 16, v36
	v_and_b32_e32 v125, 0xffff0000, v36
	v_lshlrev_b32_e32 v126, 16, v37
	v_and_b32_e32 v127, 0xffff0000, v37
	v_lshlrev_b32_e32 v128, 16, v38
	v_and_b32_e32 v129, 0xffff0000, v38
	v_lshlrev_b32_e32 v130, 16, v39
	v_and_b32_e32 v131, 0xffff0000, v39
	v_pk_mul_f32 v[116:117], v[114:115], v[116:117] op_sel_hi:[0,1]
	v_pk_mul_f32 v[118:119], v[114:115], v[118:119] op_sel_hi:[0,1]
	v_pk_mul_f32 v[120:121], v[114:115], v[120:121] op_sel_hi:[0,1]
	v_pk_mul_f32 v[122:123], v[114:115], v[122:123] op_sel_hi:[0,1]
	v_pk_mul_f32 v[124:125], v[114:115], v[124:125] op_sel_hi:[0,1]
	v_pk_mul_f32 v[126:127], v[114:115], v[126:127] op_sel_hi:[0,1]
	v_pk_mul_f32 v[128:129], v[114:115], v[128:129] op_sel_hi:[0,1]
	v_pk_mul_f32 v[130:131], v[114:115], v[130:131] op_sel_hi:[0,1]
	v_pk_mul_f32 v[132:133], v[8:9], v[116:117]
	v_pk_mul_f32 v[134:135], v[10:11], v[118:119]
	v_pk_mul_f32 v[136:137], v[12:13], v[120:121]
	v_pk_mul_f32 v[138:139], v[14:15], v[122:123]
	v_pk_mul_f32 v[140:141], v[16:17], v[124:125]
	v_pk_mul_f32 v[142:143], v[18:19], v[126:127]
	v_pk_mul_f32 v[144:145], v[20:21], v[128:129]
	v_pk_mul_f32 v[146:147], v[22:23], v[130:131]
	global_store_dwordx4 v2, v[132:135], s[34:35] offset:0 sc1
	global_store_dwordx4 v2, v[136:139], s[34:35] offset:1024 sc1
	global_store_dwordx4 v2, v[140:143], s[34:35] offset:2048 sc1
	global_store_dwordx4 v2, v[144:147], s[34:35] offset:3072 sc1
	s_branch .Lfin_tail
